# w_down share of the weight conversion moved from P4 to the workgroups idle in P6 (bx >= 136), via P4's own conversion code in conversion-only mode
# speedup vs baseline: 1.0124x; 1.0124x over previous
; __global__ void __launch_bounds__(NWAVES * 64, 2) mk_fwd(Args args) {
;     ...
;     if (IN(4)) {
;         const int NCONV = (CONV_OVERLAP && G >= 128) ? 51 : 0;
;         if (bx < NCONV) convert_weights<false, true>(P, lds, bx * NWAVES + wave, NCONV * NWAVES, wave, lane, 0, (CONV_OVERLAP && G >= 192) ? LATE_SPLIT : 0x7fffffff);
;         else {
;             sb_phase(lds, PROJ, (bf16*)(ws + WS_MIX), (const float*)(ws + WS_RSB), P.sbo_norm, bx - NCONV, G - NCONV, tid);
;             ret_out_phase(lds, PROJ, (bf16*)(ws + WS_MIX), (const bf16*)(ws + WS_ST), P.ret_norm, bx - NCONV, G - NCONV, tid);
;         }
;         if (NCONV == 0) convert_weights<false>(P, lds, gw, NGW, wave, lane);
.LBB0_519:
	s_mov_b32 s98, 0
	s_mov_b32 s99, 0
	s_mov_b32 s100, s80
	s_mov_b32 s101, s56
	s_mov_b32 s0, 0x6e00
	v_writelane_b32 v255, s0, 2
	s_mov_b32 s0, 0
	v_writelane_b32 v255, s0, 3
.Lp4_conv_entry:
	s_load_dwordx16 s[8:23], s[70:71], 0x40
	s_cmp_lt_i32 s74, 5
	s_cselect_b64 s[0:1], -1, 0
	s_and_b64 s[70:71], s[0:1], s[4:5]
	s_andn2_b64 vcc, exec, s[70:71]
	s_waitcnt lgkmcnt(0)
	v_writelane_b32 v254, s8, 18
	s_nop 1
	v_writelane_b32 v254, s9, 19
	v_writelane_b32 v254, s10, 20
	v_writelane_b32 v254, s11, 21
	v_writelane_b32 v254, s12, 22
	v_writelane_b32 v254, s13, 23
	v_writelane_b32 v254, s14, 24
	v_writelane_b32 v254, s15, 25
	v_writelane_b32 v254, s16, 26
	v_writelane_b32 v254, s17, 27
	v_writelane_b32 v254, s18, 28
	v_writelane_b32 v254, s19, 29
	v_writelane_b32 v254, s20, 30
	v_writelane_b32 v254, s21, 31
	v_writelane_b32 v254, s22, 32
	v_writelane_b32 v254, s23, 33
	s_cbranch_vccnz .LBB0_728
	s_cmp_lg_u32 s99, 0
	s_cbranch_scc1 .LBB0_558
	s_movk_i32 s0, 0x80
	v_readfirstlane_b32 s3, v0
	v_cmp_gt_u32_e32 vcc, s0, v0
	s_and_saveexec_b64 s[0:1], vcc
	s_cbranch_execz .LBB0_523
	v_lshlrev_b32_e32 v2, 2, v0
	global_load_dword v3, v2, s[50:51]
	v_add_u32_e32 v2, 0, v2
	v_add_u32_e32 v2, 0x16880, v2
	s_waitcnt vmcnt(0)
	ds_write_b32 v2, v3

; #define LAS __attribute__((address_space(3)))
; #define LAS __attribute__((address_space(3)))
;     LAS unsigned* scr = (LAS unsigned*)(lds + wave * 16384);
;     WItem d0, d1; WRegs R0, R1;
;     constexpr int KB_ = DM / 32;
;     constexpr int NALL = EARLY ? KB_ * (INW / 128) : KB_ * (DM / 128) + KB_ * (CW / 128) + KB_ * (2 * CW / 128) + (CW / 32) * (DM / 128) + KB_ * (DFF2 / 128) + (DFF / 32) * (DM / 128);
;     const int hi_all = it_hi < NALL ? it_hi : NALL, total = hi_all - it_lo, nwgs = NGW / NWAVES, chunk = (((total + nwgs - 1) / nwgs) + NWAVES - 1) / NWAVES * NWAVES;
;     int it = it_lo + (gw / NWAVES) * chunk + (gw % NWAVES); const int wend0 = it_lo + (gw / NWAVES + 1) * chunk, wend = wend0 < hi_all ? wend0 : hi_all;
.LBB0_558:
	s_abs_i32 s0, s100
	v_cvt_f32_u32_e32 v2, s0
	s_sub_i32 s4, 0, s0
	v_readlane_b32 s1, v255, 2
	s_nop 3
	s_add_i32 s1, s1, s100
	s_add_i32 s1, s1, -1
	s_xor_b32 s3, s1, s100
	v_rcp_iflag_f32_e32 v2, v2
	s_abs_i32 s1, s1
	s_ashr_i32 s3, s3, 31
	v_mul_f32_e32 v2, 0x4f7ffffe, v2
	v_cvt_u32_f32_e32 v2, v2
	s_nop 0
	v_readfirstlane_b32 s5, v2
	s_mul_i32 s4, s4, s5
	s_mul_hi_u32 s4, s5, s4
	s_add_i32 s5, s5, s4
	s_mul_hi_u32 s4, s1, s5
	s_mul_i32 s5, s4, s0
	s_sub_i32 s1, s1, s5
	s_add_i32 s6, s4, 1
	s_sub_i32 s5, s1, s0
	s_cmp_ge_u32 s1, s0
	s_cselect_b32 s4, s6, s4
	s_cselect_b32 s1, s5, s1
	s_add_i32 s5, s4, 1
	s_cmp_ge_u32 s1, s0
	s_cselect_b32 s0, s5, s4
	s_xor_b32 s0, s0, s3
	s_sub_i32 s0, s0, s3
	s_add_i32 s0, s0, 7
	s_ashr_i32 s1, s101, 31
	s_ashr_i32 s3, s0, 31
	s_lshr_b32 s1, s1, 29
	s_lshr_b32 s3, s3, 29
	s_add_i32 s0, s0, s3
	s_add_i32 s1, s101, s1
	s_and_b32 s0, s0, -8
	s_ashr_i32 s3, s1, 3
	s_and_b32 s1, s1, -8
	s_mul_i32 s3, s0, s3
	s_sub_i32 s1, s101, s1
	s_add_i32 s33, s3, s1
	s_add_i32 s3, s3, s0
	v_readlane_b32 s0, v255, 2
	v_readlane_b32 s1, v255, 3
	s_nop 3
	s_min_i32 s3, s3, s0
	s_add_i32 s3, s3, s1
	s_add_i32 s33, s33, s1
	s_cmp_lt_i32 s33, s3
	s_cselect_b64 s[4:5], -1, 0
	s_cmp_ge_i32 s33, s3
	s_cbranch_scc1 .LBB0_565
	s_cmpk_gt_i32 s33, 0xfff
	s_cbranch_scc0 .LBB0_566
	s_cmpk_gt_u32 s33, 0x11ff
	s_cbranch_scc0 .LBB0_567
	s_cmpk_gt_u32 s33, 0x15ff
	s_cbranch_scc0 .LBB0_568
	s_cmpk_gt_u32 s33, 0x17ff
	s_cbranch_scc0 .LBB0_569
	s_cmpk_gt_u32 s33, 0x6dff
	s_cbranch_scc0 .LBB0_570
	s_and_b32 s0, s33, 0x7fffffe0
	s_add_i32 s14, s0, 0xffff9200
	s_add_u32 s12, s84, 0x10800000
	s_addc_u32 s13, s85, 0
	s_lshl_b32 s0, s33, 7
	s_and_b32 s44, s0, 0xf80
	s_mov_b64 s[0:1], 0
	s_mov_b64 s[10:11], 0
	s_mov_b64 s[8:9], s[76:77]
	s_branch .LBB0_571

; __global__ void __launch_bounds__(NWAVES * 64, 2) mk_fwd(Args args) {
;     ...
;         if (NCONV == 0) convert_weights<false>(P, lds, gw, NGW, wave, lane);
;         __syncthreads();
.LBB0_727:
	s_waitcnt vmcnt(0) lgkmcnt(0)
	s_barrier
	s_cmp_lg_u32 s98, 0
	s_cbranch_scc1 .Lp6_conv_ret

; __global__ void __launch_bounds__(NWAVES * 64, 2) mk_fwd(Args args) {
;     ...
;         if (CONV_OVERLAP && G >= 192 && bx >= G / 2 + 8) { __syncthreads(); convert_weights<false, true>(P, lds, (bx - (G / 2 + 8)) * NWAVES + wave, (G - (G / 2 + 8)) * NWAVES, wave, lane, LATE_SPLIT, 0x7fffffff); }
.LBB0_925:
	s_cmpk_lt_i32 s2, 0x88
	s_cbranch_scc1 .Lp6_hook_done
	v_writelane_b32 v255, s8, 8
	v_writelane_b32 v255, s9, 9
	v_writelane_b32 v255, s12, 10
	v_writelane_b32 v255, s16, 11
	v_writelane_b32 v255, s18, 12
	v_writelane_b32 v255, s19, 13
	v_writelane_b32 v255, s20, 14
	v_writelane_b32 v255, s21, 15
	v_writelane_b32 v255, s23, 16
	v_writelane_b32 v255, s24, 17
	v_writelane_b32 v255, s26, 18
	v_writelane_b32 v255, s34, 19
	v_readlane_b32 s70, v254, 0
	v_readlane_b32 s71, v254, 1
	v_and_b32_e32 v1, 63, v0
	v_readfirstlane_b32 s101, v0
	s_sub_u32 s100, s2, 0x88
	s_lshl_b32 s100, s100, 3
	s_sub_u32 s70, s70, 0xc0
	s_subb_u32 s71, s71, 0
	s_lshr_b32 s101, s101, 6
	s_add_u32 s101, s101, s100
	s_mov_b32 s100, 120
	s_mov_b32 s0, 0x2b00
	v_writelane_b32 v255, s0, 2
	s_mov_b32 s0, 0x6e00
	v_writelane_b32 v255, s0, 3
	s_mov_b32 s98, 1
	s_mov_b32 s99, 1
	s_mov_b64 s[4:5], -1
	s_branch .Lp4_conv_entry
.Lp6_conv_ret:
	v_readlane_b32 s8, v255, 8
	v_readlane_b32 s9, v255, 9
	v_readlane_b32 s12, v255, 10
	v_readlane_b32 s16, v255, 11
	v_readlane_b32 s18, v255, 12
	v_readlane_b32 s19, v255, 13
	v_readlane_b32 s20, v255, 14
	v_readlane_b32 s21, v255, 15
	v_readlane_b32 s23, v255, 16
	v_readlane_b32 s24, v255, 17
	v_readlane_b32 s26, v255, 18
	v_readlane_b32 s34, v255, 19
	s_mov_b32 s98, 0
	s_mov_b32 s99, 0
	s_nop 3

; __global__ void __launch_bounds__(NWAVES * 64, 2) mk_fwd(Args args) {
	.amdhsa_kernel _Z6mk_fwd4Args
		.amdhsa_group_segment_fixed_size 0
		.amdhsa_private_segment_fixed_size 0
		.amdhsa_kernarg_size 448
		.amdhsa_user_sgpr_count 2
		.amdhsa_user_sgpr_dispatch_ptr 0
		.amdhsa_user_sgpr_queue_ptr 0
		.amdhsa_user_sgpr_kernarg_segment_ptr 1
		.amdhsa_user_sgpr_dispatch_id 0
		.amdhsa_user_sgpr_kernarg_preload_length 0
		.amdhsa_user_sgpr_kernarg_preload_offset 0
		.amdhsa_user_sgpr_private_segment_size 0
		.amdhsa_uses_dynamic_stack 0
		.amdhsa_enable_private_segment 0
		.amdhsa_system_sgpr_workgroup_id_x 1
		.amdhsa_system_sgpr_workgroup_id_y 0
		.amdhsa_system_sgpr_workgroup_id_z 0
		.amdhsa_system_sgpr_workgroup_info 0
		.amdhsa_system_vgpr_workitem_id 0
		.amdhsa_next_free_vgpr 256
		.amdhsa_next_free_sgpr 102
		.amdhsa_accum_offset 256
		.amdhsa_reserve_vcc 1
		.amdhsa_float_round_mode_32 0
		.amdhsa_float_round_mode_16_64 0
		.amdhsa_float_denorm_mode_32 3
		.amdhsa_float_denorm_mode_16_64 3
		.amdhsa_dx10_clamp 1
		.amdhsa_ieee_mode 1
		.amdhsa_fp16_overflow 0
		.amdhsa_tg_split 0
		.amdhsa_exception_fp_ieee_invalid_op 0
		.amdhsa_exception_fp_denorm_src 0
		.amdhsa_exception_fp_ieee_div_zero 0
		.amdhsa_exception_fp_ieee_overflow 0
		.amdhsa_exception_fp_ieee_underflow 0
		.amdhsa_exception_fp_ieee_inexact 0
		.amdhsa_exception_int_div_zero 0
	.end_amdhsa_kernel

; __global__ void __launch_bounds__(NWAVES * 64, 2) mk_fwd(Args args) {
amdhsa.kernels:
  - .agpr_count:     0
    .args:
      - .offset:         0
        .size:           192
        .value_kind:     by_value
      - .offset:         192
        .size:           4
        .value_kind:     hidden_block_count_x
      - .offset:         196
        .size:           4
        .value_kind:     hidden_block_count_y
      - .offset:         200
        .size:           4
        .value_kind:     hidden_block_count_z
      - .offset:         204
        .size:           2
        .value_kind:     hidden_group_size_x
      - .offset:         206
        .size:           2
        .value_kind:     hidden_group_size_y
      - .offset:         208
        .size:           2
        .value_kind:     hidden_group_size_z
      - .offset:         210
        .size:           2
        .value_kind:     hidden_remainder_x
      - .offset:         212
        .size:           2
        .value_kind:     hidden_remainder_y
      - .offset:         214
        .size:           2
        .value_kind:     hidden_remainder_z
      - .offset:         232
        .size:           8
        .value_kind:     hidden_global_offset_x
      - .offset:         240
        .size:           8
        .value_kind:     hidden_global_offset_y
      - .offset:         248
        .size:           8
        .value_kind:     hidden_global_offset_z
      - .offset:         256
        .size:           2
        .value_kind:     hidden_grid_dims
      - .offset:         312
        .size:           4
        .value_kind:     hidden_dynamic_lds_size
    .group_segment_fixed_size: 0
    .kernarg_segment_align: 8
    .kernarg_segment_size: 448
    .language:       OpenCL C
    .language_version:
      - 2
      - 0
    .max_flat_workgroup_size: 512
    .name:           _Z6mk_fwd4Args
    .private_segment_fixed_size: 0
    .sgpr_count:     108
    .sgpr_spill_count: 34
    .symbol:         _Z6mk_fwd4Args.kd
    .uniform_work_group_size: 1
    .uses_dynamic_stack: false
    .vgpr_count:     256
    .vgpr_spill_count: 0
    .wavefront_size: 64
